# dense up-GEMM epilogue: all in-place accumulator i32-to-f32 conversions issued ahead of the row-scale wait (extends the earlier partial hoist)
# speedup vs baseline: 1.0001x; 1.0001x over previous
.LBB0_1376:
	v_cvt_f32_i32_e32 v123, v123
	v_cvt_f32_i32_e32 v122, v122
	v_cvt_f32_i32_e32 v125, v125
	v_cvt_f32_i32_e32 v124, v124
	v_cvt_f32_i32_e32 v119, v119
	v_cvt_f32_i32_e32 v118, v118
	v_cvt_f32_i32_e32 v121, v121
	v_cvt_f32_i32_e32 v120, v120
	v_cvt_f32_i32_e32 v127, v127
	v_cvt_f32_i32_e32 v126, v126
	v_cvt_f32_i32_e32 v129, v129
	v_cvt_f32_i32_e32 v128, v128
	v_cvt_f32_i32_e32 v107, v107
	v_cvt_f32_i32_e32 v106, v106
	v_cvt_f32_i32_e32 v109, v109
	v_cvt_f32_i32_e32 v108, v108
	v_cvt_f32_i32_e32 v103, v103
	v_cvt_f32_i32_e32 v102, v102
	v_cvt_f32_i32_e32 v105, v105
	v_cvt_f32_i32_e32 v104, v104
	v_cvt_f32_i32_e32 v113, v113
	v_cvt_f32_i32_e32 v112, v112
	v_cvt_f32_i32_e32 v111, v111
	v_cvt_f32_i32_e32 v110, v110
	v_cvt_f32_i32_e32 v91, v91
	v_cvt_f32_i32_e32 v90, v90
	v_cvt_f32_i32_e32 v93, v93
	v_cvt_f32_i32_e32 v92, v92
	v_cvt_f32_i32_e32 v87, v87
	v_cvt_f32_i32_e32 v86, v86
	v_cvt_f32_i32_e32 v89, v89
	v_cvt_f32_i32_e32 v88, v88
	v_cvt_f32_i32_e32 v97, v97
	v_cvt_f32_i32_e32 v96, v96
	v_cvt_f32_i32_e32 v95, v95
	v_cvt_f32_i32_e32 v94, v94
	v_cvt_f32_i32_e32 v75, v75
	v_cvt_f32_i32_e32 v74, v74
	v_cvt_f32_i32_e32 v77, v77
	v_cvt_f32_i32_e32 v76, v76
	v_cvt_f32_i32_e32 v71, v71
	v_cvt_f32_i32_e32 v70, v70
	v_cvt_f32_i32_e32 v73, v73
	v_cvt_f32_i32_e32 v72, v72
	v_cvt_f32_i32_e32 v81, v81
	v_cvt_f32_i32_e32 v80, v80
	v_cvt_f32_i32_e32 v79, v79
	v_cvt_f32_i32_e32 v78, v78
	v_cvt_f32_i32_e32 v59, v59
	v_cvt_f32_i32_e32 v58, v58
	v_cvt_f32_i32_e32 v61, v61
	v_cvt_f32_i32_e32 v60, v60
	v_cvt_f32_i32_e32 v55, v55
	v_cvt_f32_i32_e32 v54, v54
	v_cvt_f32_i32_e32 v57, v57
	v_cvt_f32_i32_e32 v56, v56
	v_cvt_f32_i32_e32 v65, v65
	v_cvt_f32_i32_e32 v64, v64
	v_cvt_f32_i32_e32 v63, v63
	v_cvt_f32_i32_e32 v62, v62
	v_cvt_f32_i32_e32 v43, v43
	v_cvt_f32_i32_e32 v42, v42
	v_cvt_f32_i32_e32 v45, v45
	v_cvt_f32_i32_e32 v44, v44
	v_cvt_f32_i32_e32 v39, v39
	v_cvt_f32_i32_e32 v38, v38
	v_cvt_f32_i32_e32 v41, v41
	v_cvt_f32_i32_e32 v40, v40
	v_cvt_f32_i32_e32 v49, v49
	v_cvt_f32_i32_e32 v48, v48
	v_cvt_f32_i32_e32 v47, v47
	v_cvt_f32_i32_e32 v46, v46
	v_cvt_f32_i32_e32 v27, v27
	v_cvt_f32_i32_e32 v26, v26
	v_cvt_f32_i32_e32 v29, v29
	v_cvt_f32_i32_e32 v28, v28
	v_cvt_f32_i32_e32 v23, v23
	v_cvt_f32_i32_e32 v22, v22
	v_cvt_f32_i32_e32 v25, v25
	v_cvt_f32_i32_e32 v24, v24
	v_cvt_f32_i32_e32 v33, v33
	v_cvt_f32_i32_e32 v32, v32
	v_cvt_f32_i32_e32 v31, v31
	v_cvt_f32_i32_e32 v30, v30
	v_cvt_f32_i32_e32 v11, v11
	v_cvt_f32_i32_e32 v10, v10
	v_cvt_f32_i32_e32 v13, v13
	v_cvt_f32_i32_e32 v12, v12
	v_cvt_f32_i32_e32 v7, v7
	v_cvt_f32_i32_e32 v6, v6
	v_cvt_f32_i32_e32 v9, v9
	v_cvt_f32_i32_e32 v8, v8
	v_cvt_f32_i32_e32 v17, v17
	v_cvt_f32_i32_e32 v16, v16
	v_cvt_f32_i32_e32 v15, v15
	v_cvt_f32_i32_e32 v14, v14
	s_waitcnt vmcnt(0)
	v_mul_f32_e32 v164, 0x3a800000, v141
	v_mul_f32_e32 v152, 0xbfb8aa3b, v164
	v_pk_mul_f32 v[156:157], v[152:153], v[122:123] op_sel_hi:[0,1]
	v_pk_mul_f32 v[154:155], v[152:153], v[124:125] op_sel_hi:[0,1]
	v_pk_mul_f32 v[158:159], v[152:153], v[120:121] op_sel_hi:[0,1]
	v_pk_mul_f32 v[152:153], v[152:153], v[118:119] op_sel_hi:[0,1]
	v_exp_f32_e32 v156, v156
	v_exp_f32_e32 v157, v157
	v_exp_f32_e32 v152, v152
	v_exp_f32_e32 v153, v153
	v_exp_f32_e32 v154, v154
	v_exp_f32_e32 v155, v155
	s_mul_hi_i32 s4, s44, 0x2e8ba2e9
	v_exp_f32_e32 v158, v158
	v_exp_f32_e32 v159, v159
	s_lshr_b32 s5, s4, 31
	s_lshr_b32 s4, s4, 2
	s_add_i32 s4, s4, s5
	v_cvt_f32_i32_e32 v161, v117
	v_cvt_f32_i32_e32 v160, v116
	v_pk_add_f32 v[116:117], v[156:157], 1.0 op_sel_hi:[1,0]
	s_mul_i32 s4, s4, 22


	v_cvt_f32_i32_e32 v163, v115
	v_cvt_f32_i32_e32 v162, v114
	v_pk_add_f32 v[114:115], v[154:155], 1.0 op_sel_hi:[1,0]
	v_pk_add_f32 v[152:153], v[152:153], 1.0 op_sel_hi:[1,0]
	v_rcp_f32_e32 v116, v116
	v_rcp_f32_e32 v117, v117
	s_sub_i32 s4, s44, s4


	v_pk_add_f32 v[154:155], v[158:159], 1.0 op_sel_hi:[1,0]
	v_rcp_f32_e32 v152, v152
	v_rcp_f32_e32 v153, v153
	v_rcp_f32_e32 v114, v114
	v_rcp_f32_e32 v115, v115
	v_ashrrev_i32_e32 v140, 1, v140
	s_lshl_b32 s4, s4, 7
	v_rcp_f32_e32 v154, v154
	v_rcp_f32_e32 v155, v155
	v_and_b32_e32 v140, -8, v140
	s_or_b32 s4, s4, s41
	v_mul_f32_e32 v156, v164, v164
	v_add_u32_e32 v140, s4, v140
	v_pk_mul_f32 v[122:123], v[122:123], v[126:127]
	v_pk_mul_f32 v[116:117], v[156:157], v[116:117] op_sel_hi:[0,1]
	v_readlane_b32 s4, v255, 23
	v_pk_mul_f32 v[124:125], v[124:125], v[128:129]
	v_pk_mul_f32 v[114:115], v[156:157], v[114:115] op_sel_hi:[0,1]
	v_pk_mul_f32 v[116:117], v[122:123], v[116:117]
	v_pk_mul_f32 v[122:123], v[118:119], v[162:163]
	v_pk_mul_f32 v[118:119], v[120:121], v[160:161]
	v_pk_mul_f32 v[120:121], v[156:157], v[152:153] op_sel_hi:[0,1]
	v_readlane_b32 s5, v255, 24
	v_pk_mul_f32 v[114:115], v[124:125], v[114:115]
	v_pk_mul_f32 v[124:125], v[156:157], v[154:155] op_sel_hi:[0,1]
	v_pk_mul_f32 v[120:121], v[122:123], v[120:121]
	v_cndmask_b32_e64 v122, 0, 1, s[4:5]
	v_readlane_b32 s62, v255, 11
	v_readlane_b32 s78, v255, 13
	v_ashrrev_i32_e32 v141, 31, v140
	v_pk_mul_f32 v[118:119], v[118:119], v[124:125]
	v_cmp_ne_u32_e64 s[10:11], 1, v122
	s_andn2_b64 vcc, exec, s[4:5]
	s_mov_b64 s[26:27], -1
	v_readlane_b32 s63, v255, 12
	v_readlane_b32 s79, v255, 14
	s_movk_i32 s19, 0xb00
	s_movk_i32 s21, 0x1600
	s_movk_i32 s74, 0x1000
	s_cbranch_vccnz .LBB0_1378
	v_max_f32_e32 v122, v116, v116
	v_med3_f32 v123, v122, s61, v237
	v_max_f32_e32 v122, v117, v117
	v_med3_f32 v124, v122, s61, v237
	v_mov_b32_e32 v122, v1
	v_cvt_pk_fp8_f32 v122, v123, v124
	v_max_f32_e32 v125, v114, v114
	v_max_f32_e32 v124, v115, v115
	v_med3_f32 v123, v125, s61, v237
	v_med3_f32 v124, v124, s61, v237
	v_cvt_pk_fp8_f32 v122, v123, v124 op_sel:[0,0,1]
	v_max_f32_e32 v123, v120, v120
	v_med3_f32 v124, v123, s61, v237
	v_max_f32_e32 v123, v121, v121
	v_med3_f32 v125, v123, s61, v237
	v_mov_b32_e32 v123, v1
	v_cvt_pk_fp8_f32 v123, v124, v125
	v_max_f32_e32 v126, v118, v118
	v_max_f32_e32 v125, v119, v119
	v_med3_f32 v124, v126, s61, v237
	v_med3_f32 v125, v125, s61, v237
	v_cvt_pk_fp8_f32 v123, v124, v125 op_sel:[0,0,1]
	v_mov_b64_e32 v[124:125], s[12:13]
	v_mad_i64_i32 v[124:125], s[4:5], v142, s19, v[124:125]
	v_lshl_add_u64 v[124:125], v[124:125], 0, v[140:141]
	s_mov_b64 s[26:27], 0
	global_store_dwordx2 v[124:125], v[122:123], off

.LBB0_1380:


	v_mul_f32_e32 v115, 0x3a800000, v151
	v_mul_f32_e32 v116, 0xbfb8aa3b, v115
	v_pk_mul_f32 v[118:119], v[116:117], v[108:109] op_sel_hi:[0,1]
	v_pk_mul_f32 v[120:121], v[116:117], v[106:107] op_sel_hi:[0,1]
	v_pk_mul_f32 v[122:123], v[116:117], v[104:105] op_sel_hi:[0,1]
	v_pk_mul_f32 v[116:117], v[116:117], v[102:103] op_sel_hi:[0,1]
	v_exp_f32_e32 v120, v120
	v_exp_f32_e32 v121, v121
	v_exp_f32_e32 v118, v118
	v_exp_f32_e32 v119, v119
	v_exp_f32_e32 v116, v116
	v_exp_f32_e32 v117, v117
	v_exp_f32_e32 v122, v122
	v_exp_f32_e32 v123, v123
	v_cvt_f32_i32_e32 v125, v101
	v_cvt_f32_i32_e32 v124, v100
	v_cvt_f32_i32_e32 v127, v99
	v_cvt_f32_i32_e32 v126, v98
	v_pk_add_f32 v[98:99], v[118:119], 1.0 op_sel_hi:[1,0]
	v_pk_add_f32 v[100:101], v[120:121], 1.0 op_sel_hi:[1,0]


	v_pk_add_f32 v[118:119], v[122:123], 1.0 op_sel_hi:[1,0]
	v_pk_add_f32 v[116:117], v[116:117], 1.0 op_sel_hi:[1,0]
	v_rcp_f32_e32 v100, v100
	v_rcp_f32_e32 v101, v101
	v_rcp_f32_e32 v98, v98
	v_rcp_f32_e32 v99, v99
	v_rcp_f32_e32 v116, v116
	v_rcp_f32_e32 v117, v117
	v_rcp_f32_e32 v118, v118
	v_rcp_f32_e32 v119, v119
	v_mul_f32_e32 v120, v115, v115
	v_pk_mul_f32 v[106:107], v[106:107], v[110:111]
	v_pk_mul_f32 v[108:109], v[108:109], v[112:113]
	v_pk_mul_f32 v[100:101], v[120:121], v[100:101] op_sel_hi:[0,1]
	v_pk_mul_f32 v[98:99], v[120:121], v[98:99] op_sel_hi:[0,1]
	v_pk_mul_f32 v[98:99], v[108:109], v[98:99]
	v_pk_mul_f32 v[100:101], v[106:107], v[100:101]
	v_pk_mul_f32 v[106:107], v[102:103], v[126:127]
	v_pk_mul_f32 v[102:103], v[104:105], v[124:125]
	v_pk_mul_f32 v[104:105], v[120:121], v[116:117] op_sel_hi:[0,1]
	v_pk_mul_f32 v[108:109], v[120:121], v[118:119] op_sel_hi:[0,1]
	v_or_b32_e32 v114, 16, v142
	v_pk_mul_f32 v[102:103], v[102:103], v[108:109]
	v_pk_mul_f32 v[104:105], v[106:107], v[104:105]
	s_and_b64 vcc, exec, s[10:11]
	s_mov_b64 s[26:27], -1
	s_cbranch_vccnz .LBB0_1382
	v_max_f32_e32 v106, v100, v100
	v_med3_f32 v107, v106, s61, v237
	v_max_f32_e32 v106, v101, v101
	v_med3_f32 v108, v106, s61, v237
	v_mov_b32_e32 v106, v1
	v_cvt_pk_fp8_f32 v106, v107, v108
	v_max_f32_e32 v109, v98, v98
	v_max_f32_e32 v108, v99, v99
	v_med3_f32 v107, v109, s61, v237
	v_med3_f32 v108, v108, s61, v237
	v_cvt_pk_fp8_f32 v106, v107, v108 op_sel:[0,0,1]
	v_max_f32_e32 v107, v104, v104
	v_med3_f32 v108, v107, s61, v237
	v_max_f32_e32 v107, v105, v105
	v_med3_f32 v109, v107, s61, v237
	v_mov_b32_e32 v107, v1
	v_cvt_pk_fp8_f32 v107, v108, v109
	v_max_f32_e32 v110, v102, v102
	v_max_f32_e32 v109, v103, v103
	v_med3_f32 v108, v110, s61, v237
	v_med3_f32 v109, v109, s61, v237
	v_cvt_pk_fp8_f32 v107, v108, v109 op_sel:[0,0,1]
	v_mov_b64_e32 v[108:109], s[12:13]
	v_mad_i64_i32 v[108:109], s[4:5], v114, s19, v[108:109]
	v_lshl_add_u64 v[108:109], v[108:109], 0, v[140:141]
	s_mov_b64 s[26:27], 0
	global_store_dwordx2 v[108:109], v[106:107], off

.LBB0_1384:


	v_mul_f32_e32 v99, 0x3a800000, v150
	v_mul_f32_e32 v100, 0xbfb8aa3b, v99
	v_pk_mul_f32 v[102:103], v[100:101], v[92:93] op_sel_hi:[0,1]
	v_pk_mul_f32 v[104:105], v[100:101], v[90:91] op_sel_hi:[0,1]
	v_pk_mul_f32 v[106:107], v[100:101], v[88:89] op_sel_hi:[0,1]
	v_pk_mul_f32 v[100:101], v[100:101], v[86:87] op_sel_hi:[0,1]
	v_exp_f32_e32 v104, v104
	v_exp_f32_e32 v105, v105
	v_exp_f32_e32 v102, v102
	v_exp_f32_e32 v103, v103
	v_exp_f32_e32 v100, v100
	v_exp_f32_e32 v101, v101
	v_exp_f32_e32 v106, v106
	v_exp_f32_e32 v107, v107
	v_cvt_f32_i32_e32 v109, v85
	v_cvt_f32_i32_e32 v108, v84
	v_cvt_f32_i32_e32 v111, v83
	v_cvt_f32_i32_e32 v110, v82
	v_pk_add_f32 v[82:83], v[102:103], 1.0 op_sel_hi:[1,0]
	v_pk_add_f32 v[84:85], v[104:105], 1.0 op_sel_hi:[1,0]


	v_pk_add_f32 v[102:103], v[106:107], 1.0 op_sel_hi:[1,0]
	v_pk_add_f32 v[100:101], v[100:101], 1.0 op_sel_hi:[1,0]
	v_rcp_f32_e32 v84, v84
	v_rcp_f32_e32 v85, v85
	v_rcp_f32_e32 v82, v82
	v_rcp_f32_e32 v83, v83
	v_rcp_f32_e32 v100, v100
	v_rcp_f32_e32 v101, v101
	v_rcp_f32_e32 v102, v102
	v_rcp_f32_e32 v103, v103
	v_mul_f32_e32 v104, v99, v99
	v_pk_mul_f32 v[90:91], v[90:91], v[94:95]
	v_pk_mul_f32 v[92:93], v[92:93], v[96:97]
	v_pk_mul_f32 v[84:85], v[104:105], v[84:85] op_sel_hi:[0,1]
	v_pk_mul_f32 v[82:83], v[104:105], v[82:83] op_sel_hi:[0,1]
	v_pk_mul_f32 v[82:83], v[92:93], v[82:83]
	v_pk_mul_f32 v[84:85], v[90:91], v[84:85]
	v_pk_mul_f32 v[90:91], v[86:87], v[110:111]
	v_pk_mul_f32 v[86:87], v[88:89], v[108:109]
	v_pk_mul_f32 v[88:89], v[104:105], v[100:101] op_sel_hi:[0,1]
	v_pk_mul_f32 v[92:93], v[104:105], v[102:103] op_sel_hi:[0,1]
	v_or_b32_e32 v98, 32, v142
	v_pk_mul_f32 v[86:87], v[86:87], v[92:93]
	v_pk_mul_f32 v[88:89], v[90:91], v[88:89]
	s_and_b64 vcc, exec, s[10:11]
	s_mov_b64 s[26:27], -1
	s_cbranch_vccnz .LBB0_1386
	v_max_f32_e32 v90, v84, v84
	v_med3_f32 v91, v90, s61, v237
	v_max_f32_e32 v90, v85, v85
	v_med3_f32 v92, v90, s61, v237
	v_mov_b32_e32 v90, v1
	v_cvt_pk_fp8_f32 v90, v91, v92
	v_max_f32_e32 v93, v82, v82
	v_max_f32_e32 v92, v83, v83
	v_med3_f32 v91, v93, s61, v237
	v_med3_f32 v92, v92, s61, v237
	v_cvt_pk_fp8_f32 v90, v91, v92 op_sel:[0,0,1]
	v_max_f32_e32 v91, v88, v88
	v_med3_f32 v92, v91, s61, v237
	v_max_f32_e32 v91, v89, v89
	v_med3_f32 v93, v91, s61, v237
	v_mov_b32_e32 v91, v1
	v_cvt_pk_fp8_f32 v91, v92, v93
	v_max_f32_e32 v94, v86, v86
	v_max_f32_e32 v93, v87, v87
	v_med3_f32 v92, v94, s61, v237
	v_med3_f32 v93, v93, s61, v237
	v_cvt_pk_fp8_f32 v91, v92, v93 op_sel:[0,0,1]
	v_mov_b64_e32 v[92:93], s[12:13]
	v_mad_i64_i32 v[92:93], s[4:5], v98, s19, v[92:93]
	v_lshl_add_u64 v[92:93], v[92:93], 0, v[140:141]
	s_mov_b64 s[26:27], 0
	global_store_dwordx2 v[92:93], v[90:91], off

.LBB0_1388:


	v_mul_f32_e32 v83, 0x3a800000, v149
	v_mul_f32_e32 v84, 0xbfb8aa3b, v83
	v_pk_mul_f32 v[86:87], v[84:85], v[76:77] op_sel_hi:[0,1]
	v_pk_mul_f32 v[88:89], v[84:85], v[74:75] op_sel_hi:[0,1]
	v_pk_mul_f32 v[90:91], v[84:85], v[72:73] op_sel_hi:[0,1]
	v_pk_mul_f32 v[84:85], v[84:85], v[70:71] op_sel_hi:[0,1]
	v_exp_f32_e32 v88, v88
	v_exp_f32_e32 v89, v89
	v_exp_f32_e32 v86, v86
	v_exp_f32_e32 v87, v87
	v_exp_f32_e32 v84, v84
	v_exp_f32_e32 v85, v85
	v_exp_f32_e32 v90, v90
	v_exp_f32_e32 v91, v91
	v_cvt_f32_i32_e32 v93, v69
	v_cvt_f32_i32_e32 v92, v68
	v_cvt_f32_i32_e32 v95, v67
	v_cvt_f32_i32_e32 v94, v66
	v_pk_add_f32 v[66:67], v[86:87], 1.0 op_sel_hi:[1,0]
	v_pk_add_f32 v[68:69], v[88:89], 1.0 op_sel_hi:[1,0]


	v_pk_add_f32 v[86:87], v[90:91], 1.0 op_sel_hi:[1,0]
	v_pk_add_f32 v[84:85], v[84:85], 1.0 op_sel_hi:[1,0]
	v_rcp_f32_e32 v68, v68
	v_rcp_f32_e32 v69, v69
	v_rcp_f32_e32 v66, v66
	v_rcp_f32_e32 v67, v67
	v_rcp_f32_e32 v84, v84
	v_rcp_f32_e32 v85, v85
	v_rcp_f32_e32 v86, v86
	v_rcp_f32_e32 v87, v87
	v_mul_f32_e32 v88, v83, v83
	v_pk_mul_f32 v[74:75], v[74:75], v[78:79]
	v_pk_mul_f32 v[76:77], v[76:77], v[80:81]
	v_pk_mul_f32 v[68:69], v[88:89], v[68:69] op_sel_hi:[0,1]
	v_pk_mul_f32 v[66:67], v[88:89], v[66:67] op_sel_hi:[0,1]
	v_pk_mul_f32 v[66:67], v[76:77], v[66:67]
	v_pk_mul_f32 v[68:69], v[74:75], v[68:69]
	v_pk_mul_f32 v[74:75], v[70:71], v[94:95]
	v_pk_mul_f32 v[70:71], v[72:73], v[92:93]
	v_pk_mul_f32 v[72:73], v[88:89], v[84:85] op_sel_hi:[0,1]
	v_pk_mul_f32 v[76:77], v[88:89], v[86:87] op_sel_hi:[0,1]
	v_or_b32_e32 v82, 48, v142
	v_pk_mul_f32 v[70:71], v[70:71], v[76:77]
	v_pk_mul_f32 v[72:73], v[74:75], v[72:73]
	s_and_b64 vcc, exec, s[10:11]
	s_mov_b64 s[26:27], -1
	s_cbranch_vccnz .LBB0_1390
	v_max_f32_e32 v74, v68, v68
	v_med3_f32 v75, v74, s61, v237
	v_max_f32_e32 v74, v69, v69
	v_med3_f32 v76, v74, s61, v237
	v_mov_b32_e32 v74, v1
	v_cvt_pk_fp8_f32 v74, v75, v76
	v_max_f32_e32 v77, v66, v66
	v_max_f32_e32 v76, v67, v67
	v_med3_f32 v75, v77, s61, v237
	v_med3_f32 v76, v76, s61, v237
	v_cvt_pk_fp8_f32 v74, v75, v76 op_sel:[0,0,1]
	v_max_f32_e32 v75, v72, v72
	v_med3_f32 v76, v75, s61, v237
	v_max_f32_e32 v75, v73, v73
	v_med3_f32 v77, v75, s61, v237
	v_mov_b32_e32 v75, v1
	v_cvt_pk_fp8_f32 v75, v76, v77
	v_max_f32_e32 v78, v70, v70
	v_max_f32_e32 v77, v71, v71
	v_med3_f32 v76, v78, s61, v237
	v_med3_f32 v77, v77, s61, v237
	v_cvt_pk_fp8_f32 v75, v76, v77 op_sel:[0,0,1]
	v_mov_b64_e32 v[76:77], s[12:13]
	v_mad_i64_i32 v[76:77], s[4:5], v82, s19, v[76:77]
	v_lshl_add_u64 v[76:77], v[76:77], 0, v[140:141]
	s_mov_b64 s[26:27], 0
	global_store_dwordx2 v[76:77], v[74:75], off

.LBB0_1392:


	v_mul_f32_e32 v67, 0x3a800000, v148
	v_mul_f32_e32 v68, 0xbfb8aa3b, v67
	v_pk_mul_f32 v[70:71], v[68:69], v[60:61] op_sel_hi:[0,1]
	v_pk_mul_f32 v[72:73], v[68:69], v[58:59] op_sel_hi:[0,1]
	v_pk_mul_f32 v[74:75], v[68:69], v[56:57] op_sel_hi:[0,1]
	v_pk_mul_f32 v[68:69], v[68:69], v[54:55] op_sel_hi:[0,1]
	v_exp_f32_e32 v72, v72
	v_exp_f32_e32 v73, v73
	v_exp_f32_e32 v70, v70
	v_exp_f32_e32 v71, v71
	v_exp_f32_e32 v68, v68
	v_exp_f32_e32 v69, v69
	v_exp_f32_e32 v74, v74
	v_exp_f32_e32 v75, v75
	v_cvt_f32_i32_e32 v77, v53
	v_cvt_f32_i32_e32 v76, v52
	v_cvt_f32_i32_e32 v79, v51
	v_cvt_f32_i32_e32 v78, v50
	v_pk_add_f32 v[50:51], v[70:71], 1.0 op_sel_hi:[1,0]
	v_pk_add_f32 v[52:53], v[72:73], 1.0 op_sel_hi:[1,0]


	v_pk_add_f32 v[70:71], v[74:75], 1.0 op_sel_hi:[1,0]
	v_pk_add_f32 v[68:69], v[68:69], 1.0 op_sel_hi:[1,0]
	v_rcp_f32_e32 v52, v52
	v_rcp_f32_e32 v53, v53
	v_rcp_f32_e32 v50, v50
	v_rcp_f32_e32 v51, v51
	v_rcp_f32_e32 v68, v68
	v_rcp_f32_e32 v69, v69
	v_rcp_f32_e32 v70, v70
	v_rcp_f32_e32 v71, v71
	v_mul_f32_e32 v72, v67, v67
	v_pk_mul_f32 v[58:59], v[58:59], v[62:63]
	v_pk_mul_f32 v[60:61], v[60:61], v[64:65]
	v_pk_mul_f32 v[52:53], v[72:73], v[52:53] op_sel_hi:[0,1]
	v_pk_mul_f32 v[50:51], v[72:73], v[50:51] op_sel_hi:[0,1]
	v_pk_mul_f32 v[50:51], v[60:61], v[50:51]
	v_pk_mul_f32 v[52:53], v[58:59], v[52:53]
	v_pk_mul_f32 v[58:59], v[54:55], v[78:79]
	v_pk_mul_f32 v[54:55], v[56:57], v[76:77]
	v_pk_mul_f32 v[56:57], v[72:73], v[68:69] op_sel_hi:[0,1]
	v_pk_mul_f32 v[60:61], v[72:73], v[70:71] op_sel_hi:[0,1]
	v_add_u32_e32 v66, 0x80, v142
	v_pk_mul_f32 v[54:55], v[54:55], v[60:61]
	v_pk_mul_f32 v[56:57], v[58:59], v[56:57]
	s_and_b64 vcc, exec, s[10:11]
	s_mov_b64 s[26:27], -1
	s_cbranch_vccnz .LBB0_1394
	v_max_f32_e32 v58, v52, v52
	v_med3_f32 v59, v58, s61, v237
	v_max_f32_e32 v58, v53, v53
	v_med3_f32 v60, v58, s61, v237
	v_mov_b32_e32 v58, v1
	v_cvt_pk_fp8_f32 v58, v59, v60
	v_max_f32_e32 v61, v50, v50
	v_max_f32_e32 v60, v51, v51
	v_med3_f32 v59, v61, s61, v237
	v_med3_f32 v60, v60, s61, v237
	v_cvt_pk_fp8_f32 v58, v59, v60 op_sel:[0,0,1]
	v_max_f32_e32 v59, v56, v56
	v_med3_f32 v60, v59, s61, v237
	v_max_f32_e32 v59, v57, v57
	v_med3_f32 v61, v59, s61, v237
	v_mov_b32_e32 v59, v1
	v_cvt_pk_fp8_f32 v59, v60, v61
	v_max_f32_e32 v62, v54, v54
	v_max_f32_e32 v61, v55, v55
	v_med3_f32 v60, v62, s61, v237
	v_med3_f32 v61, v61, s61, v237
	v_cvt_pk_fp8_f32 v59, v60, v61 op_sel:[0,0,1]
	v_mov_b64_e32 v[60:61], s[12:13]
	v_mad_i64_i32 v[60:61], s[4:5], v66, s19, v[60:61]
	v_lshl_add_u64 v[60:61], v[60:61], 0, v[140:141]
	s_mov_b64 s[26:27], 0
	global_store_dwordx2 v[60:61], v[58:59], off

.LBB0_1396:


	v_mul_f32_e32 v51, 0x3a800000, v147
	v_mul_f32_e32 v52, 0xbfb8aa3b, v51
	v_pk_mul_f32 v[54:55], v[52:53], v[44:45] op_sel_hi:[0,1]
	v_pk_mul_f32 v[56:57], v[52:53], v[42:43] op_sel_hi:[0,1]
	v_pk_mul_f32 v[58:59], v[52:53], v[40:41] op_sel_hi:[0,1]
	v_pk_mul_f32 v[52:53], v[52:53], v[38:39] op_sel_hi:[0,1]
	v_exp_f32_e32 v56, v56
	v_exp_f32_e32 v57, v57
	v_exp_f32_e32 v54, v54
	v_exp_f32_e32 v55, v55
	v_exp_f32_e32 v52, v52
	v_exp_f32_e32 v53, v53
	v_exp_f32_e32 v58, v58
	v_exp_f32_e32 v59, v59
	v_cvt_f32_i32_e32 v61, v37
	v_cvt_f32_i32_e32 v60, v36
	v_cvt_f32_i32_e32 v63, v35
	v_cvt_f32_i32_e32 v62, v34
	v_pk_add_f32 v[34:35], v[54:55], 1.0 op_sel_hi:[1,0]
	v_pk_add_f32 v[36:37], v[56:57], 1.0 op_sel_hi:[1,0]


	v_pk_add_f32 v[54:55], v[58:59], 1.0 op_sel_hi:[1,0]
	v_pk_add_f32 v[52:53], v[52:53], 1.0 op_sel_hi:[1,0]
	v_rcp_f32_e32 v36, v36
	v_rcp_f32_e32 v37, v37
	v_rcp_f32_e32 v34, v34
	v_rcp_f32_e32 v35, v35
	v_rcp_f32_e32 v52, v52
	v_rcp_f32_e32 v53, v53
	v_rcp_f32_e32 v54, v54
	v_rcp_f32_e32 v55, v55
	v_mul_f32_e32 v56, v51, v51
	v_pk_mul_f32 v[42:43], v[42:43], v[46:47]
	v_pk_mul_f32 v[44:45], v[44:45], v[48:49]
	v_pk_mul_f32 v[36:37], v[56:57], v[36:37] op_sel_hi:[0,1]
	v_pk_mul_f32 v[34:35], v[56:57], v[34:35] op_sel_hi:[0,1]
	v_pk_mul_f32 v[34:35], v[44:45], v[34:35]
	v_pk_mul_f32 v[36:37], v[42:43], v[36:37]
	v_pk_mul_f32 v[42:43], v[38:39], v[62:63]
	v_pk_mul_f32 v[38:39], v[40:41], v[60:61]
	v_pk_mul_f32 v[40:41], v[56:57], v[52:53] op_sel_hi:[0,1]
	v_pk_mul_f32 v[44:45], v[56:57], v[54:55] op_sel_hi:[0,1]
	v_add_u32_e32 v50, 0x90, v142
	v_pk_mul_f32 v[38:39], v[38:39], v[44:45]
	v_pk_mul_f32 v[40:41], v[42:43], v[40:41]
	s_and_b64 vcc, exec, s[10:11]
	s_mov_b64 s[26:27], -1
	s_cbranch_vccnz .LBB0_1398
	v_max_f32_e32 v42, v36, v36
	v_med3_f32 v43, v42, s61, v237
	v_max_f32_e32 v42, v37, v37
	v_med3_f32 v44, v42, s61, v237
	v_mov_b32_e32 v42, v1
	v_cvt_pk_fp8_f32 v42, v43, v44
	v_max_f32_e32 v45, v34, v34
	v_max_f32_e32 v44, v35, v35
	v_med3_f32 v43, v45, s61, v237
	v_med3_f32 v44, v44, s61, v237
	v_cvt_pk_fp8_f32 v42, v43, v44 op_sel:[0,0,1]
	v_max_f32_e32 v43, v40, v40
	v_med3_f32 v44, v43, s61, v237
	v_max_f32_e32 v43, v41, v41
	v_med3_f32 v45, v43, s61, v237
	v_mov_b32_e32 v43, v1
	v_cvt_pk_fp8_f32 v43, v44, v45
	v_max_f32_e32 v46, v38, v38
	v_max_f32_e32 v45, v39, v39
	v_med3_f32 v44, v46, s61, v237
	v_med3_f32 v45, v45, s61, v237
	v_cvt_pk_fp8_f32 v43, v44, v45 op_sel:[0,0,1]
	v_mov_b64_e32 v[44:45], s[12:13]
	v_mad_i64_i32 v[44:45], s[4:5], v50, s19, v[44:45]
	v_lshl_add_u64 v[44:45], v[44:45], 0, v[140:141]
	s_mov_b64 s[26:27], 0
	global_store_dwordx2 v[44:45], v[42:43], off

.LBB0_1400:


	v_mul_f32_e32 v35, 0x3a800000, v146
	v_mul_f32_e32 v36, 0xbfb8aa3b, v35
	v_pk_mul_f32 v[38:39], v[36:37], v[28:29] op_sel_hi:[0,1]
	v_pk_mul_f32 v[40:41], v[36:37], v[26:27] op_sel_hi:[0,1]
	v_pk_mul_f32 v[42:43], v[36:37], v[24:25] op_sel_hi:[0,1]
	v_pk_mul_f32 v[36:37], v[36:37], v[22:23] op_sel_hi:[0,1]
	v_exp_f32_e32 v40, v40
	v_exp_f32_e32 v41, v41
	v_exp_f32_e32 v38, v38
	v_exp_f32_e32 v39, v39
	v_exp_f32_e32 v36, v36
	v_exp_f32_e32 v37, v37
	v_exp_f32_e32 v42, v42
	v_exp_f32_e32 v43, v43
	v_cvt_f32_i32_e32 v45, v21
	v_cvt_f32_i32_e32 v44, v20
	v_cvt_f32_i32_e32 v47, v19
	v_cvt_f32_i32_e32 v46, v18
	v_pk_add_f32 v[18:19], v[38:39], 1.0 op_sel_hi:[1,0]
	v_pk_add_f32 v[20:21], v[40:41], 1.0 op_sel_hi:[1,0]


	v_pk_add_f32 v[38:39], v[42:43], 1.0 op_sel_hi:[1,0]
	v_pk_add_f32 v[36:37], v[36:37], 1.0 op_sel_hi:[1,0]
	v_rcp_f32_e32 v20, v20
	v_rcp_f32_e32 v21, v21
	v_rcp_f32_e32 v18, v18
	v_rcp_f32_e32 v19, v19
	v_rcp_f32_e32 v36, v36
	v_rcp_f32_e32 v37, v37
	v_rcp_f32_e32 v38, v38
	v_rcp_f32_e32 v39, v39
	v_mul_f32_e32 v40, v35, v35
	v_pk_mul_f32 v[26:27], v[26:27], v[30:31]
	v_pk_mul_f32 v[28:29], v[28:29], v[32:33]
	v_pk_mul_f32 v[20:21], v[40:41], v[20:21] op_sel_hi:[0,1]
	v_pk_mul_f32 v[18:19], v[40:41], v[18:19] op_sel_hi:[0,1]
	v_pk_mul_f32 v[18:19], v[28:29], v[18:19]
	v_pk_mul_f32 v[20:21], v[26:27], v[20:21]
	v_pk_mul_f32 v[26:27], v[22:23], v[46:47]
	v_pk_mul_f32 v[22:23], v[24:25], v[44:45]
	v_pk_mul_f32 v[24:25], v[40:41], v[36:37] op_sel_hi:[0,1]
	v_pk_mul_f32 v[28:29], v[40:41], v[38:39] op_sel_hi:[0,1]
	v_add_u32_e32 v34, 0xa0, v142
	v_pk_mul_f32 v[22:23], v[22:23], v[28:29]
	v_pk_mul_f32 v[24:25], v[26:27], v[24:25]
	s_and_b64 vcc, exec, s[10:11]
	s_mov_b64 s[26:27], -1
	s_cbranch_vccnz .LBB0_1402
	v_max_f32_e32 v26, v20, v20
	v_med3_f32 v27, v26, s61, v237
	v_max_f32_e32 v26, v21, v21
	v_med3_f32 v28, v26, s61, v237
	v_mov_b32_e32 v26, v1
	v_cvt_pk_fp8_f32 v26, v27, v28
	v_max_f32_e32 v29, v18, v18
	v_max_f32_e32 v28, v19, v19
	v_med3_f32 v27, v29, s61, v237
	v_med3_f32 v28, v28, s61, v237
	v_cvt_pk_fp8_f32 v26, v27, v28 op_sel:[0,0,1]
	v_max_f32_e32 v27, v24, v24
	v_med3_f32 v28, v27, s61, v237
	v_max_f32_e32 v27, v25, v25
	v_med3_f32 v29, v27, s61, v237
	v_mov_b32_e32 v27, v1
	v_cvt_pk_fp8_f32 v27, v28, v29
	v_max_f32_e32 v30, v22, v22
	v_max_f32_e32 v29, v23, v23
	v_med3_f32 v28, v30, s61, v237
	v_med3_f32 v29, v29, s61, v237
	v_cvt_pk_fp8_f32 v27, v28, v29 op_sel:[0,0,1]
	v_mov_b64_e32 v[28:29], s[12:13]
	v_mad_i64_i32 v[28:29], s[4:5], v34, s19, v[28:29]
	v_lshl_add_u64 v[28:29], v[28:29], 0, v[140:141]
	s_mov_b64 s[26:27], 0
	global_store_dwordx2 v[28:29], v[26:27], off

.LBB0_1404:


	v_mul_f32_e32 v19, 0x3a800000, v143
	v_mul_f32_e32 v20, 0xbfb8aa3b, v19
	v_pk_mul_f32 v[22:23], v[20:21], v[12:13] op_sel_hi:[0,1]
	v_pk_mul_f32 v[24:25], v[20:21], v[10:11] op_sel_hi:[0,1]
	v_pk_mul_f32 v[26:27], v[20:21], v[8:9] op_sel_hi:[0,1]
	v_pk_mul_f32 v[20:21], v[20:21], v[6:7] op_sel_hi:[0,1]
	v_exp_f32_e32 v24, v24
	v_exp_f32_e32 v25, v25
	v_exp_f32_e32 v22, v22
	v_exp_f32_e32 v23, v23
	v_exp_f32_e32 v20, v20
	v_exp_f32_e32 v21, v21
	v_exp_f32_e32 v26, v26
	v_exp_f32_e32 v27, v27
	v_cvt_f32_i32_e32 v29, v5
	v_cvt_f32_i32_e32 v28, v4
	v_cvt_f32_i32_e32 v31, v3
	v_cvt_f32_i32_e32 v30, v2
	v_pk_add_f32 v[2:3], v[22:23], 1.0 op_sel_hi:[1,0]
	v_pk_add_f32 v[4:5], v[24:25], 1.0 op_sel_hi:[1,0]


	v_pk_add_f32 v[22:23], v[26:27], 1.0 op_sel_hi:[1,0]
	v_pk_add_f32 v[20:21], v[20:21], 1.0 op_sel_hi:[1,0]
	v_rcp_f32_e32 v4, v4
	v_rcp_f32_e32 v5, v5
	v_rcp_f32_e32 v2, v2
	v_rcp_f32_e32 v3, v3
	v_rcp_f32_e32 v20, v20
	v_rcp_f32_e32 v21, v21
	v_rcp_f32_e32 v22, v22
	v_rcp_f32_e32 v23, v23
	v_mul_f32_e32 v24, v19, v19
	v_pk_mul_f32 v[10:11], v[10:11], v[14:15]
	v_pk_mul_f32 v[12:13], v[12:13], v[16:17]
	v_pk_mul_f32 v[4:5], v[24:25], v[4:5] op_sel_hi:[0,1]
	v_pk_mul_f32 v[2:3], v[24:25], v[2:3] op_sel_hi:[0,1]
	v_pk_mul_f32 v[2:3], v[12:13], v[2:3]
	v_pk_mul_f32 v[4:5], v[10:11], v[4:5]
	v_pk_mul_f32 v[10:11], v[6:7], v[30:31]
	v_pk_mul_f32 v[6:7], v[8:9], v[28:29]
	v_pk_mul_f32 v[8:9], v[24:25], v[20:21] op_sel_hi:[0,1]
	v_pk_mul_f32 v[12:13], v[24:25], v[22:23] op_sel_hi:[0,1]
	v_add_u32_e32 v18, 0xb0, v142
	v_pk_mul_f32 v[6:7], v[6:7], v[12:13]
	v_pk_mul_f32 v[8:9], v[10:11], v[8:9]
	s_and_b64 vcc, exec, s[10:11]
	s_mov_b64 s[10:11], -1
	s_cbranch_vccnz .LBB0_1407
	v_max_f32_e32 v10, v4, v4
	v_med3_f32 v11, v10, s61, v237
	v_max_f32_e32 v10, v5, v5
	v_med3_f32 v12, v10, s61, v237
	v_mov_b32_e32 v10, v1
	v_cvt_pk_fp8_f32 v10, v11, v12
	v_max_f32_e32 v13, v2, v2
	v_max_f32_e32 v12, v3, v3
	v_med3_f32 v11, v13, s61, v237
	v_med3_f32 v12, v12, s61, v237
	v_cvt_pk_fp8_f32 v10, v11, v12 op_sel:[0,0,1]
	v_max_f32_e32 v11, v8, v8
	v_med3_f32 v12, v11, s61, v237
	v_max_f32_e32 v11, v9, v9
	v_med3_f32 v13, v11, s61, v237
	v_mov_b32_e32 v11, v1
	v_cvt_pk_fp8_f32 v11, v12, v13
	v_max_f32_e32 v14, v6, v6
	v_max_f32_e32 v13, v7, v7
	v_med3_f32 v12, v14, s61, v237
	v_med3_f32 v13, v13, s61, v237
	v_cvt_pk_fp8_f32 v11, v12, v13 op_sel:[0,0,1]
	v_mov_b64_e32 v[12:13], s[12:13]
	v_mad_i64_i32 v[12:13], s[4:5], v18, s19, v[12:13]
	v_lshl_add_u64 v[12:13], v[12:13], 0, v[140:141]
	global_store_dwordx2 v[12:13], v[10:11], off
	s_cbranch_execz .LBB0_1408
